# scan wave instruction stream kept 8-byte aligned (e64 fmac encodings, each s_waitcnt paired with an s_nop 0), one wait fewer per pair-step
# baseline (speedup 1.0000x reference)
; #define LAS __attribute__((address_space(3)))
; __device__ __forceinline__ void scan_head(const Params& p, LAS unsigned char* lds, int bh, const int wave) {
;     ...
;         if (wave < 4) {
;             __builtin_amdgcn_s_setprio(3);
;             const int bp = chunk & 1, vb = chunk % 3;
;             const LAS unsigned char* awp = lds + L_AW + bp * 8192 + sel * 128 + rg * 16;
;             const LAS unsigned char* wwp = lds + L_W + bp * 8192 + rg * 16;
;             const LAS unsigned char* abp = lds + L_BK + bp * 16384 + rg * 256 + ri * 4;
;             const LAS unsigned char* vp = lds + L_V + vb * 8192 + (16 * wave + ri) * 4;
;             const LAS unsigned char* csp = lds + L_CS + bp * 256;
;             LAS unsigned char* yp = (rg == 0) ? (lds + L_Y + bp * 8192 + (16 * wave + ri) * 4) : ((rg == 2) ? (lds + L_Y + bp * 8192 + 256 + (16 * wave + ri) * 4) : (lds + L_DUMMY + tid * 4));
;             const int y_st = (rg & 1) ? 0 : 512;
;     ...
;             bf16x8 Pa0, Pa1, Qa0, Qa1; f32x4 Pw0, Pw1, Pw2, Pw3, Qw0, Qw1, Qw2, Qw3, Pcs, Qcs; float Pb0, Pb1, Pb2, Pb3, Pvt, Pvu, Qb0, Qb1, Qb2, Qb3, Qvt, Qvu;
;             SCAN_LD(P, 0);
; #pragma unroll 1
;             for (int pi = 0; pi < 16; pi += 2) {
;                 SCAN_LD(Q, pi + 1);
;                 SCAN_STEP(P, pi);
;                 if (pi + 2 < 16) SCAN_LD(P, pi + 2);
;                 SCAN_STEP(Q, pi + 1);
.LBB0_806:
	s_and_b64 vcc, exec, s[14:15]
	s_cbranch_vccz .LBB0_789
	s_setprio 3
	s_and_b32 s2, s51, 1
	s_lshl_b32 s15, s2, 13
	s_mul_i32 s14, s51, 0xab
	s_lshl_b32 s52, s2, 14
	s_bfe_u32 s14, s14, 0x70009
	s_lshl_b32 s44, s2, 8
	s_mul_i32 s14, s14, 3
	s_waitcnt vmcnt(0)
	s_sub_i32 s14, s51, s14
	s_and_b32 s14, s14, 0xff
	s_lshl_b32 s14, s14, 13
	s_add_i32 s44, s44, 0x20300
	v_add_u32_e32 v98, s15, v176
	v_add_u32_e32 v99, s15, v175
	v_add_u32_e32 v0, s52, v178
	v_add_u32_e32 v1, s14, v179
	v_add_u32_e32 v0, 0x8000, v0
	v_add_u32_e32 v4, 0x100, v1
	v_mov_b32_e32 v2, s44
	v_cndmask_b32_e64 v4, v4, v1, s[8:9]
	v_cndmask_b32_e64 v4, v4, v1, s[12:13]
	v_cndmask_b32_e64 v1, v4, v1, s[10:11]
	v_add_u32_e32 v4, s15, v181
	v_add_u32_e32 v6, 0xd00, v180
	v_add_u32_e32 v5, 0x100, v4
	v_cndmask_b32_e64 v5, v6, v5, s[10:11]
	v_cndmask_b32_e64 v3, v5, v4, s[8:9]
	ds_read_b128 v[68:71], v98 offset:0
	ds_read_b128 v[72:75], v98 offset:64
	ds_read_b128 v[76:79], v99 offset:16384
	ds_read_b128 v[80:83], v99 offset:16448
	ds_read_b128 v[84:87], v99 offset:16512
	ds_read_b128 v[88:91], v99 offset:16576
	ds_read2_b32 v[92:93], v0 offset1:16
	ds_read2_b32 v[94:95], v0 offset0:32 offset1:48
	ds_read_b32 v96, v1 offset:0
	ds_read_b128 v[100:103], v2 offset:0
	v_cvt_pk_bf16_f32 v8, v64, v65
	v_cvt_pk_bf16_f32 v9, v66, v67
	v_cvt_pk_bf16_f32 v10, v60, v61
	v_cvt_pk_bf16_f32 v11, v62, v63
	v_cvt_pk_bf16_f32 v12, v52, v53
	v_cvt_pk_bf16_f32 v13, v54, v55
	s_waitcnt lgkmcnt(4)
	s_nop 0
	v_mfma_f32_16x16x32_bf16 v[140:143], v[68:71], v[8:11], 0
	v_cvt_pk_bf16_f32 v14, v56, v57
	v_cvt_pk_bf16_f32 v15, v58, v59
	v_pk_mul_f32 v[64:65], v[64:65], v[76:77]
	v_pk_mul_f32 v[66:67], v[66:67], v[78:79]
	v_mfma_f32_16x16x32_bf16 v[140:143], v[72:75], v[12:15], v[140:143]
	v_pk_mul_f32 v[60:61], v[60:61], v[80:81]
	v_pk_mul_f32 v[62:63], v[62:63], v[82:83]
	v_pk_mul_f32 v[52:53], v[52:53], v[84:85]
	v_pk_mul_f32 v[54:55], v[54:55], v[86:87]
	v_pk_mul_f32 v[56:57], v[56:57], v[88:89]
	v_pk_mul_f32 v[58:59], v[58:59], v[90:91]
	ds_read_b128 v[104:107], v98 offset:512
	ds_read_b128 v[108:111], v98 offset:576
	ds_read_b128 v[112:115], v99 offset:16640
	ds_read_b128 v[116:119], v99 offset:16704
	ds_read_b128 v[120:123], v99 offset:16768
	ds_read_b128 v[128:131], v99 offset:16832
	s_waitcnt lgkmcnt(6)
	s_nop 0
	v_fma_f32 v144, v100, v140, v142
	v_fmac_f32_e64 v144, v101, v96
	v_cndmask_b32_e64 v145, v96, v144, s[10:11]
	v_cndmask_b32_e64 v145, v145, v140, s[8:9]
	v_fma_f32 v50, v102, v140, v143
	v_fmac_f32_e64 v50, v103, v96
	v_mfma_f32_16x16x4_f32 v[64:67], v92, v145, v[64:67]
	v_mfma_f32_16x16x4_f32 v[60:63], v93, v145, v[60:63]
	v_mfma_f32_16x16x4_f32 v[52:55], v94, v145, v[52:55]
	v_mfma_f32_16x16x4_f32 v[56:59], v95, v145, v[56:59]
	v_cndmask_b32_e64 v50, v50, v141, s[8:9]
	ds_write_b32 v3, v50 offset:0
	v_add_u32_e32 v0, 0x400, v0
	ds_read2_b32 v[132:133], v0 offset1:16
	ds_read2_b32 v[134:135], v0 offset0:32 offset1:48
	ds_read_b32 v97, v1 offset:512
	ds_read_b128 v[136:139], v2 offset:16
	v_cvt_pk_bf16_f32 v8, v64, v65
	v_cvt_pk_bf16_f32 v9, v66, v67
	v_cvt_pk_bf16_f32 v10, v60, v61
	v_cvt_pk_bf16_f32 v11, v62, v63
	v_cvt_pk_bf16_f32 v12, v52, v53
	v_cvt_pk_bf16_f32 v13, v54, v55
	s_waitcnt lgkmcnt(4)
	s_nop 0
	v_mfma_f32_16x16x32_bf16 v[140:143], v[104:107], v[8:11], 0
	v_cvt_pk_bf16_f32 v14, v56, v57
	v_cvt_pk_bf16_f32 v15, v58, v59
	v_pk_mul_f32 v[64:65], v[64:65], v[112:113]
	v_pk_mul_f32 v[66:67], v[66:67], v[114:115]
	v_mfma_f32_16x16x32_bf16 v[140:143], v[108:111], v[12:15], v[140:143]
	v_pk_mul_f32 v[60:61], v[60:61], v[116:117]
	v_pk_mul_f32 v[62:63], v[62:63], v[118:119]
	v_pk_mul_f32 v[52:53], v[52:53], v[120:121]
	v_pk_mul_f32 v[54:55], v[54:55], v[122:123]
	v_pk_mul_f32 v[56:57], v[56:57], v[128:129]
	v_pk_mul_f32 v[58:59], v[58:59], v[130:131]
	ds_read_b128 v[68:71], v98 offset:1024
	ds_read_b128 v[72:75], v98 offset:1088
	ds_read_b128 v[76:79], v99 offset:16896
	ds_read_b128 v[80:83], v99 offset:16960
	ds_read_b128 v[84:87], v99 offset:17024
	ds_read_b128 v[88:91], v99 offset:17088
	s_waitcnt lgkmcnt(6)
	s_nop 0
	v_fma_f32 v144, v136, v140, v142
	v_fmac_f32_e64 v144, v137, v97
	v_cndmask_b32_e64 v145, v97, v144, s[10:11]
	v_cndmask_b32_e64 v145, v145, v140, s[8:9]
	v_fma_f32 v50, v138, v140, v143
	v_fmac_f32_e64 v50, v139, v97
	v_mfma_f32_16x16x4_f32 v[64:67], v132, v145, v[64:67]
	v_mfma_f32_16x16x4_f32 v[60:63], v133, v145, v[60:63]
	v_mfma_f32_16x16x4_f32 v[52:55], v134, v145, v[52:55]
	v_mfma_f32_16x16x4_f32 v[56:59], v135, v145, v[56:59]
	v_cndmask_b32_e64 v50, v50, v141, s[8:9]
	ds_write_b32 v3, v50 offset:512
	v_add_u32_e32 v0, 0x400, v0
	ds_read2_b32 v[92:93], v0 offset1:16
	ds_read2_b32 v[94:95], v0 offset0:32 offset1:48
	ds_read_b32 v96, v1 offset:1024
	ds_read_b128 v[100:103], v2 offset:32
	v_cvt_pk_bf16_f32 v8, v64, v65
	v_cvt_pk_bf16_f32 v9, v66, v67
	v_cvt_pk_bf16_f32 v10, v60, v61
	v_cvt_pk_bf16_f32 v11, v62, v63
	v_cvt_pk_bf16_f32 v12, v52, v53
	v_cvt_pk_bf16_f32 v13, v54, v55
	s_waitcnt lgkmcnt(4)
	s_nop 0
	v_mfma_f32_16x16x32_bf16 v[140:143], v[68:71], v[8:11], 0
	v_cvt_pk_bf16_f32 v14, v56, v57
	v_cvt_pk_bf16_f32 v15, v58, v59
	v_pk_mul_f32 v[64:65], v[64:65], v[76:77]
	v_pk_mul_f32 v[66:67], v[66:67], v[78:79]
	v_mfma_f32_16x16x32_bf16 v[140:143], v[72:75], v[12:15], v[140:143]
	v_pk_mul_f32 v[60:61], v[60:61], v[80:81]
	v_pk_mul_f32 v[62:63], v[62:63], v[82:83]
	v_pk_mul_f32 v[52:53], v[52:53], v[84:85]
	v_pk_mul_f32 v[54:55], v[54:55], v[86:87]
	v_pk_mul_f32 v[56:57], v[56:57], v[88:89]
	v_pk_mul_f32 v[58:59], v[58:59], v[90:91]
	ds_read_b128 v[104:107], v98 offset:1536
	ds_read_b128 v[108:111], v98 offset:1600
	ds_read_b128 v[112:115], v99 offset:17152
	ds_read_b128 v[116:119], v99 offset:17216
	ds_read_b128 v[120:123], v99 offset:17280
	ds_read_b128 v[128:131], v99 offset:17344
	s_waitcnt lgkmcnt(6)
; __device__ __forceinline__ void scan_head(const Params& p, LAS unsigned char* lds, int bh, const int wave) {
;     ...
;             bf16x8 Pa0, Pa1, Qa0, Qa1; f32x4 Pw0, Pw1, Pw2, Pw3, Qw0, Qw1, Qw2, Qw3, Pcs, Qcs; float Pb0, Pb1, Pb2, Pb3, Pvt, Pvu, Qb0, Qb1, Qb2, Qb3, Qvt, Qvu;
;             SCAN_LD(P, 0);
; #pragma unroll 1
;             for (int pi = 0; pi < 16; pi += 2) {
;                 SCAN_LD(Q, pi + 1);
;                 SCAN_STEP(P, pi);
;                 if (pi + 2 < 16) SCAN_LD(P, pi + 2);
;                 SCAN_STEP(Q, pi + 1);
	s_nop 0
	v_fma_f32 v144, v100, v140, v142
	v_fmac_f32_e64 v144, v101, v96
	v_cndmask_b32_e64 v145, v96, v144, s[10:11]
	v_cndmask_b32_e64 v145, v145, v140, s[8:9]
	v_fma_f32 v50, v102, v140, v143
	v_fmac_f32_e64 v50, v103, v96
	v_mfma_f32_16x16x4_f32 v[64:67], v92, v145, v[64:67]
	v_mfma_f32_16x16x4_f32 v[60:63], v93, v145, v[60:63]
	v_mfma_f32_16x16x4_f32 v[52:55], v94, v145, v[52:55]
	v_mfma_f32_16x16x4_f32 v[56:59], v95, v145, v[56:59]
	v_cndmask_b32_e64 v50, v50, v141, s[8:9]
	ds_write_b32 v3, v50 offset:1024
	v_add_u32_e32 v0, 0x400, v0
	ds_read2_b32 v[132:133], v0 offset1:16
	ds_read2_b32 v[134:135], v0 offset0:32 offset1:48
	ds_read_b32 v97, v1 offset:1536
	ds_read_b128 v[136:139], v2 offset:48
	v_cvt_pk_bf16_f32 v8, v64, v65
	v_cvt_pk_bf16_f32 v9, v66, v67
	v_cvt_pk_bf16_f32 v10, v60, v61
	v_cvt_pk_bf16_f32 v11, v62, v63
	v_cvt_pk_bf16_f32 v12, v52, v53
	v_cvt_pk_bf16_f32 v13, v54, v55
	s_waitcnt lgkmcnt(4)
	s_nop 0
	v_mfma_f32_16x16x32_bf16 v[140:143], v[104:107], v[8:11], 0
	v_cvt_pk_bf16_f32 v14, v56, v57
	v_cvt_pk_bf16_f32 v15, v58, v59
	v_pk_mul_f32 v[64:65], v[64:65], v[112:113]
	v_pk_mul_f32 v[66:67], v[66:67], v[114:115]
	v_mfma_f32_16x16x32_bf16 v[140:143], v[108:111], v[12:15], v[140:143]
	v_pk_mul_f32 v[60:61], v[60:61], v[116:117]
	v_pk_mul_f32 v[62:63], v[62:63], v[118:119]
	v_pk_mul_f32 v[52:53], v[52:53], v[120:121]
	v_pk_mul_f32 v[54:55], v[54:55], v[122:123]
	v_pk_mul_f32 v[56:57], v[56:57], v[128:129]
	v_pk_mul_f32 v[58:59], v[58:59], v[130:131]
	ds_read_b128 v[68:71], v98 offset:2048
	ds_read_b128 v[72:75], v98 offset:2112
	ds_read_b128 v[76:79], v99 offset:17408
	ds_read_b128 v[80:83], v99 offset:17472
	ds_read_b128 v[84:87], v99 offset:17536
	ds_read_b128 v[88:91], v99 offset:17600
	s_waitcnt lgkmcnt(6)
	s_nop 0
	v_fma_f32 v144, v136, v140, v142
	v_fmac_f32_e64 v144, v137, v97
	v_cndmask_b32_e64 v145, v97, v144, s[10:11]
	v_cndmask_b32_e64 v145, v145, v140, s[8:9]
	v_fma_f32 v50, v138, v140, v143
	v_fmac_f32_e64 v50, v139, v97
	v_mfma_f32_16x16x4_f32 v[64:67], v132, v145, v[64:67]
	v_mfma_f32_16x16x4_f32 v[60:63], v133, v145, v[60:63]
	v_mfma_f32_16x16x4_f32 v[52:55], v134, v145, v[52:55]
	v_mfma_f32_16x16x4_f32 v[56:59], v135, v145, v[56:59]
	v_cndmask_b32_e64 v50, v50, v141, s[8:9]
	ds_write_b32 v3, v50 offset:1536
	v_add_u32_e32 v0, 0x400, v0
	ds_read2_b32 v[92:93], v0 offset1:16
	ds_read2_b32 v[94:95], v0 offset0:32 offset1:48
	ds_read_b32 v96, v1 offset:2048
	ds_read_b128 v[100:103], v2 offset:64
	v_cvt_pk_bf16_f32 v8, v64, v65
	v_cvt_pk_bf16_f32 v9, v66, v67
	v_cvt_pk_bf16_f32 v10, v60, v61
	v_cvt_pk_bf16_f32 v11, v62, v63
	v_cvt_pk_bf16_f32 v12, v52, v53
	v_cvt_pk_bf16_f32 v13, v54, v55
	s_waitcnt lgkmcnt(4)
	s_nop 0
	v_mfma_f32_16x16x32_bf16 v[140:143], v[68:71], v[8:11], 0
	v_cvt_pk_bf16_f32 v14, v56, v57
	v_cvt_pk_bf16_f32 v15, v58, v59
	v_pk_mul_f32 v[64:65], v[64:65], v[76:77]
	v_pk_mul_f32 v[66:67], v[66:67], v[78:79]
	v_mfma_f32_16x16x32_bf16 v[140:143], v[72:75], v[12:15], v[140:143]
	v_pk_mul_f32 v[60:61], v[60:61], v[80:81]
	v_pk_mul_f32 v[62:63], v[62:63], v[82:83]
	v_pk_mul_f32 v[52:53], v[52:53], v[84:85]
	v_pk_mul_f32 v[54:55], v[54:55], v[86:87]
	v_pk_mul_f32 v[56:57], v[56:57], v[88:89]
	v_pk_mul_f32 v[58:59], v[58:59], v[90:91]
	ds_read_b128 v[104:107], v98 offset:2560
	ds_read_b128 v[108:111], v98 offset:2624
	ds_read_b128 v[112:115], v99 offset:17664
	ds_read_b128 v[116:119], v99 offset:17728
	ds_read_b128 v[120:123], v99 offset:17792
	ds_read_b128 v[128:131], v99 offset:17856
	s_waitcnt lgkmcnt(6)
	s_nop 0
	v_fma_f32 v144, v100, v140, v142
	v_fmac_f32_e64 v144, v101, v96
	v_cndmask_b32_e64 v145, v96, v144, s[10:11]
	v_cndmask_b32_e64 v145, v145, v140, s[8:9]
	v_fma_f32 v50, v102, v140, v143
	v_fmac_f32_e64 v50, v103, v96
	v_mfma_f32_16x16x4_f32 v[64:67], v92, v145, v[64:67]
	v_mfma_f32_16x16x4_f32 v[60:63], v93, v145, v[60:63]
	v_mfma_f32_16x16x4_f32 v[52:55], v94, v145, v[52:55]
	v_mfma_f32_16x16x4_f32 v[56:59], v95, v145, v[56:59]
	v_cndmask_b32_e64 v50, v50, v141, s[8:9]
	ds_write_b32 v3, v50 offset:2048
	v_add_u32_e32 v0, 0x400, v0
	ds_read2_b32 v[132:133], v0 offset1:16
	ds_read2_b32 v[134:135], v0 offset0:32 offset1:48
	ds_read_b32 v97, v1 offset:2560
	ds_read_b128 v[136:139], v2 offset:80
	v_cvt_pk_bf16_f32 v8, v64, v65
	v_cvt_pk_bf16_f32 v9, v66, v67
	v_cvt_pk_bf16_f32 v10, v60, v61
	v_cvt_pk_bf16_f32 v11, v62, v63
	v_cvt_pk_bf16_f32 v12, v52, v53
	v_cvt_pk_bf16_f32 v13, v54, v55
	s_waitcnt lgkmcnt(4)
	s_nop 0
	v_mfma_f32_16x16x32_bf16 v[140:143], v[104:107], v[8:11], 0
	v_cvt_pk_bf16_f32 v14, v56, v57
	v_cvt_pk_bf16_f32 v15, v58, v59
	v_pk_mul_f32 v[64:65], v[64:65], v[112:113]
	v_pk_mul_f32 v[66:67], v[66:67], v[114:115]
	v_mfma_f32_16x16x32_bf16 v[140:143], v[108:111], v[12:15], v[140:143]
	v_pk_mul_f32 v[60:61], v[60:61], v[116:117]
	v_pk_mul_f32 v[62:63], v[62:63], v[118:119]
	v_pk_mul_f32 v[52:53], v[52:53], v[120:121]
	v_pk_mul_f32 v[54:55], v[54:55], v[122:123]
	v_pk_mul_f32 v[56:57], v[56:57], v[128:129]
	v_pk_mul_f32 v[58:59], v[58:59], v[130:131]
	ds_read_b128 v[68:71], v98 offset:3072
	ds_read_b128 v[72:75], v98 offset:3136
	ds_read_b128 v[76:79], v99 offset:17920
	ds_read_b128 v[80:83], v99 offset:17984
	ds_read_b128 v[84:87], v99 offset:18048
	ds_read_b128 v[88:91], v99 offset:18112
	s_waitcnt lgkmcnt(6)
; __device__ __forceinline__ void scan_head(const Params& p, LAS unsigned char* lds, int bh, const int wave) {
;     ...
;             bf16x8 Pa0, Pa1, Qa0, Qa1; f32x4 Pw0, Pw1, Pw2, Pw3, Qw0, Qw1, Qw2, Qw3, Pcs, Qcs; float Pb0, Pb1, Pb2, Pb3, Pvt, Pvu, Qb0, Qb1, Qb2, Qb3, Qvt, Qvu;
;             SCAN_LD(P, 0);
; #pragma unroll 1
;             for (int pi = 0; pi < 16; pi += 2) {
;                 SCAN_LD(Q, pi + 1);
;                 SCAN_STEP(P, pi);
;                 if (pi + 2 < 16) SCAN_LD(P, pi + 2);
;                 SCAN_STEP(Q, pi + 1);
	s_nop 0
	v_fma_f32 v144, v136, v140, v142
	v_fmac_f32_e64 v144, v137, v97
	v_cndmask_b32_e64 v145, v97, v144, s[10:11]
	v_cndmask_b32_e64 v145, v145, v140, s[8:9]
	v_fma_f32 v50, v138, v140, v143
	v_fmac_f32_e64 v50, v139, v97
	v_mfma_f32_16x16x4_f32 v[64:67], v132, v145, v[64:67]
	v_mfma_f32_16x16x4_f32 v[60:63], v133, v145, v[60:63]
	v_mfma_f32_16x16x4_f32 v[52:55], v134, v145, v[52:55]
	v_mfma_f32_16x16x4_f32 v[56:59], v135, v145, v[56:59]
	v_cndmask_b32_e64 v50, v50, v141, s[8:9]
	ds_write_b32 v3, v50 offset:2560
	v_add_u32_e32 v0, 0x400, v0
	ds_read2_b32 v[92:93], v0 offset1:16
	ds_read2_b32 v[94:95], v0 offset0:32 offset1:48
	ds_read_b32 v96, v1 offset:3072
	ds_read_b128 v[100:103], v2 offset:96
	v_cvt_pk_bf16_f32 v8, v64, v65
	v_cvt_pk_bf16_f32 v9, v66, v67
	v_cvt_pk_bf16_f32 v10, v60, v61
	v_cvt_pk_bf16_f32 v11, v62, v63
	v_cvt_pk_bf16_f32 v12, v52, v53
	v_cvt_pk_bf16_f32 v13, v54, v55
	s_waitcnt lgkmcnt(4)
	s_nop 0
	v_mfma_f32_16x16x32_bf16 v[140:143], v[68:71], v[8:11], 0
	v_cvt_pk_bf16_f32 v14, v56, v57
	v_cvt_pk_bf16_f32 v15, v58, v59
	v_pk_mul_f32 v[64:65], v[64:65], v[76:77]
	v_pk_mul_f32 v[66:67], v[66:67], v[78:79]
	v_mfma_f32_16x16x32_bf16 v[140:143], v[72:75], v[12:15], v[140:143]
	v_pk_mul_f32 v[60:61], v[60:61], v[80:81]
	v_pk_mul_f32 v[62:63], v[62:63], v[82:83]
	v_pk_mul_f32 v[52:53], v[52:53], v[84:85]
	v_pk_mul_f32 v[54:55], v[54:55], v[86:87]
	v_pk_mul_f32 v[56:57], v[56:57], v[88:89]
	v_pk_mul_f32 v[58:59], v[58:59], v[90:91]
	ds_read_b128 v[104:107], v98 offset:3584
	ds_read_b128 v[108:111], v98 offset:3648
	ds_read_b128 v[112:115], v99 offset:18176
	ds_read_b128 v[116:119], v99 offset:18240
	ds_read_b128 v[120:123], v99 offset:18304
	ds_read_b128 v[128:131], v99 offset:18368
	s_waitcnt lgkmcnt(6)
	s_nop 0
	v_fma_f32 v144, v100, v140, v142
	v_fmac_f32_e64 v144, v101, v96
	v_cndmask_b32_e64 v145, v96, v144, s[10:11]
	v_cndmask_b32_e64 v145, v145, v140, s[8:9]
	v_fma_f32 v50, v102, v140, v143
	v_fmac_f32_e64 v50, v103, v96
	v_mfma_f32_16x16x4_f32 v[64:67], v92, v145, v[64:67]
	v_mfma_f32_16x16x4_f32 v[60:63], v93, v145, v[60:63]
	v_mfma_f32_16x16x4_f32 v[52:55], v94, v145, v[52:55]
	v_mfma_f32_16x16x4_f32 v[56:59], v95, v145, v[56:59]
	v_cndmask_b32_e64 v50, v50, v141, s[8:9]
	ds_write_b32 v3, v50 offset:3072
	v_add_u32_e32 v0, 0x400, v0
	ds_read2_b32 v[132:133], v0 offset1:16
	ds_read2_b32 v[134:135], v0 offset0:32 offset1:48
	ds_read_b32 v97, v1 offset:3584
	ds_read_b128 v[136:139], v2 offset:112
	v_cvt_pk_bf16_f32 v8, v64, v65
	v_cvt_pk_bf16_f32 v9, v66, v67
	v_cvt_pk_bf16_f32 v10, v60, v61
	v_cvt_pk_bf16_f32 v11, v62, v63
	v_cvt_pk_bf16_f32 v12, v52, v53
	v_cvt_pk_bf16_f32 v13, v54, v55
	s_waitcnt lgkmcnt(4)
	s_nop 0
	v_mfma_f32_16x16x32_bf16 v[140:143], v[104:107], v[8:11], 0
	v_cvt_pk_bf16_f32 v14, v56, v57
	v_cvt_pk_bf16_f32 v15, v58, v59
	v_pk_mul_f32 v[64:65], v[64:65], v[112:113]
	v_pk_mul_f32 v[66:67], v[66:67], v[114:115]
	v_mfma_f32_16x16x32_bf16 v[140:143], v[108:111], v[12:15], v[140:143]
	v_pk_mul_f32 v[60:61], v[60:61], v[116:117]
	v_pk_mul_f32 v[62:63], v[62:63], v[118:119]
	v_pk_mul_f32 v[52:53], v[52:53], v[120:121]
	v_pk_mul_f32 v[54:55], v[54:55], v[122:123]
	v_pk_mul_f32 v[56:57], v[56:57], v[128:129]
	v_pk_mul_f32 v[58:59], v[58:59], v[130:131]
	ds_read_b128 v[68:71], v98 offset:4096
	ds_read_b128 v[72:75], v98 offset:4160
	ds_read_b128 v[76:79], v99 offset:18432
	ds_read_b128 v[80:83], v99 offset:18496
	ds_read_b128 v[84:87], v99 offset:18560
	ds_read_b128 v[88:91], v99 offset:18624
	s_waitcnt lgkmcnt(6)
	s_nop 0
	v_fma_f32 v144, v136, v140, v142
	v_fmac_f32_e64 v144, v137, v97
	v_cndmask_b32_e64 v145, v97, v144, s[10:11]
	v_cndmask_b32_e64 v145, v145, v140, s[8:9]
	v_fma_f32 v50, v138, v140, v143
	v_fmac_f32_e64 v50, v139, v97
	v_mfma_f32_16x16x4_f32 v[64:67], v132, v145, v[64:67]
	v_mfma_f32_16x16x4_f32 v[60:63], v133, v145, v[60:63]
	v_mfma_f32_16x16x4_f32 v[52:55], v134, v145, v[52:55]
	v_mfma_f32_16x16x4_f32 v[56:59], v135, v145, v[56:59]
	v_cndmask_b32_e64 v50, v50, v141, s[8:9]
	ds_write_b32 v3, v50 offset:3584
	v_add_u32_e32 v0, 0x400, v0
	ds_read2_b32 v[92:93], v0 offset1:16
	ds_read2_b32 v[94:95], v0 offset0:32 offset1:48
	ds_read_b32 v96, v1 offset:4096
	ds_read_b128 v[100:103], v2 offset:128
	v_cvt_pk_bf16_f32 v8, v64, v65
	v_cvt_pk_bf16_f32 v9, v66, v67
	v_cvt_pk_bf16_f32 v10, v60, v61
	v_cvt_pk_bf16_f32 v11, v62, v63
	v_cvt_pk_bf16_f32 v12, v52, v53
	v_cvt_pk_bf16_f32 v13, v54, v55
	s_waitcnt lgkmcnt(4)
	s_nop 0
	v_mfma_f32_16x16x32_bf16 v[140:143], v[68:71], v[8:11], 0
	v_cvt_pk_bf16_f32 v14, v56, v57
	v_cvt_pk_bf16_f32 v15, v58, v59
	v_pk_mul_f32 v[64:65], v[64:65], v[76:77]
	v_pk_mul_f32 v[66:67], v[66:67], v[78:79]
	v_mfma_f32_16x16x32_bf16 v[140:143], v[72:75], v[12:15], v[140:143]
	v_pk_mul_f32 v[60:61], v[60:61], v[80:81]
	v_pk_mul_f32 v[62:63], v[62:63], v[82:83]
	v_pk_mul_f32 v[52:53], v[52:53], v[84:85]
	v_pk_mul_f32 v[54:55], v[54:55], v[86:87]
	v_pk_mul_f32 v[56:57], v[56:57], v[88:89]
	v_pk_mul_f32 v[58:59], v[58:59], v[90:91]
	ds_read_b128 v[104:107], v98 offset:4608
	ds_read_b128 v[108:111], v98 offset:4672
	ds_read_b128 v[112:115], v99 offset:18688
	ds_read_b128 v[116:119], v99 offset:18752
	ds_read_b128 v[120:123], v99 offset:18816
	ds_read_b128 v[128:131], v99 offset:18880
	s_waitcnt lgkmcnt(6)
; __device__ __forceinline__ void scan_head(const Params& p, LAS unsigned char* lds, int bh, const int wave) {
;     ...
;             bf16x8 Pa0, Pa1, Qa0, Qa1; f32x4 Pw0, Pw1, Pw2, Pw3, Qw0, Qw1, Qw2, Qw3, Pcs, Qcs; float Pb0, Pb1, Pb2, Pb3, Pvt, Pvu, Qb0, Qb1, Qb2, Qb3, Qvt, Qvu;
;             SCAN_LD(P, 0);
; #pragma unroll 1
;             for (int pi = 0; pi < 16; pi += 2) {
;                 SCAN_LD(Q, pi + 1);
;                 SCAN_STEP(P, pi);
;                 if (pi + 2 < 16) SCAN_LD(P, pi + 2);
;                 SCAN_STEP(Q, pi + 1);
	s_nop 0
	v_fma_f32 v144, v100, v140, v142
	v_fmac_f32_e64 v144, v101, v96
	v_cndmask_b32_e64 v145, v96, v144, s[10:11]
	v_cndmask_b32_e64 v145, v145, v140, s[8:9]
	v_fma_f32 v50, v102, v140, v143
	v_fmac_f32_e64 v50, v103, v96
	v_mfma_f32_16x16x4_f32 v[64:67], v92, v145, v[64:67]
	v_mfma_f32_16x16x4_f32 v[60:63], v93, v145, v[60:63]
	v_mfma_f32_16x16x4_f32 v[52:55], v94, v145, v[52:55]
	v_mfma_f32_16x16x4_f32 v[56:59], v95, v145, v[56:59]
	v_cndmask_b32_e64 v50, v50, v141, s[8:9]
	ds_write_b32 v3, v50 offset:4096
	v_add_u32_e32 v0, 0x400, v0
	ds_read2_b32 v[132:133], v0 offset1:16
	ds_read2_b32 v[134:135], v0 offset0:32 offset1:48
	ds_read_b32 v97, v1 offset:4608
	ds_read_b128 v[136:139], v2 offset:144
	v_cvt_pk_bf16_f32 v8, v64, v65
	v_cvt_pk_bf16_f32 v9, v66, v67
	v_cvt_pk_bf16_f32 v10, v60, v61
	v_cvt_pk_bf16_f32 v11, v62, v63
	v_cvt_pk_bf16_f32 v12, v52, v53
	v_cvt_pk_bf16_f32 v13, v54, v55
	s_waitcnt lgkmcnt(4)
	s_nop 0
	v_mfma_f32_16x16x32_bf16 v[140:143], v[104:107], v[8:11], 0
	v_cvt_pk_bf16_f32 v14, v56, v57
	v_cvt_pk_bf16_f32 v15, v58, v59
	v_pk_mul_f32 v[64:65], v[64:65], v[112:113]
	v_pk_mul_f32 v[66:67], v[66:67], v[114:115]
	v_mfma_f32_16x16x32_bf16 v[140:143], v[108:111], v[12:15], v[140:143]
	v_pk_mul_f32 v[60:61], v[60:61], v[116:117]
	v_pk_mul_f32 v[62:63], v[62:63], v[118:119]
	v_pk_mul_f32 v[52:53], v[52:53], v[120:121]
	v_pk_mul_f32 v[54:55], v[54:55], v[122:123]
	v_pk_mul_f32 v[56:57], v[56:57], v[128:129]
	v_pk_mul_f32 v[58:59], v[58:59], v[130:131]
	ds_read_b128 v[68:71], v98 offset:5120
	ds_read_b128 v[72:75], v98 offset:5184
	ds_read_b128 v[76:79], v99 offset:18944
	ds_read_b128 v[80:83], v99 offset:19008
	ds_read_b128 v[84:87], v99 offset:19072
	ds_read_b128 v[88:91], v99 offset:19136
	s_waitcnt lgkmcnt(6)
	s_nop 0
	v_fma_f32 v144, v136, v140, v142
	v_fmac_f32_e64 v144, v137, v97
	v_cndmask_b32_e64 v145, v97, v144, s[10:11]
	v_cndmask_b32_e64 v145, v145, v140, s[8:9]
	v_fma_f32 v50, v138, v140, v143
	v_fmac_f32_e64 v50, v139, v97
	v_mfma_f32_16x16x4_f32 v[64:67], v132, v145, v[64:67]
	v_mfma_f32_16x16x4_f32 v[60:63], v133, v145, v[60:63]
	v_mfma_f32_16x16x4_f32 v[52:55], v134, v145, v[52:55]
	v_mfma_f32_16x16x4_f32 v[56:59], v135, v145, v[56:59]
	v_cndmask_b32_e64 v50, v50, v141, s[8:9]
	ds_write_b32 v3, v50 offset:4608
	v_add_u32_e32 v0, 0x400, v0
	ds_read2_b32 v[92:93], v0 offset1:16
	ds_read2_b32 v[94:95], v0 offset0:32 offset1:48
	ds_read_b32 v96, v1 offset:5120
	ds_read_b128 v[100:103], v2 offset:160
	v_cvt_pk_bf16_f32 v8, v64, v65
	v_cvt_pk_bf16_f32 v9, v66, v67
	v_cvt_pk_bf16_f32 v10, v60, v61
	v_cvt_pk_bf16_f32 v11, v62, v63
	v_cvt_pk_bf16_f32 v12, v52, v53
	v_cvt_pk_bf16_f32 v13, v54, v55
	s_waitcnt lgkmcnt(4)
	s_nop 0
	v_mfma_f32_16x16x32_bf16 v[140:143], v[68:71], v[8:11], 0
	v_cvt_pk_bf16_f32 v14, v56, v57
	v_cvt_pk_bf16_f32 v15, v58, v59
	v_pk_mul_f32 v[64:65], v[64:65], v[76:77]
	v_pk_mul_f32 v[66:67], v[66:67], v[78:79]
	v_mfma_f32_16x16x32_bf16 v[140:143], v[72:75], v[12:15], v[140:143]
	v_pk_mul_f32 v[60:61], v[60:61], v[80:81]
	v_pk_mul_f32 v[62:63], v[62:63], v[82:83]
	v_pk_mul_f32 v[52:53], v[52:53], v[84:85]
	v_pk_mul_f32 v[54:55], v[54:55], v[86:87]
	v_pk_mul_f32 v[56:57], v[56:57], v[88:89]
	v_pk_mul_f32 v[58:59], v[58:59], v[90:91]
	ds_read_b128 v[104:107], v98 offset:5632
	ds_read_b128 v[108:111], v98 offset:5696
	ds_read_b128 v[112:115], v99 offset:19200
	ds_read_b128 v[116:119], v99 offset:19264
	ds_read_b128 v[120:123], v99 offset:19328
	ds_read_b128 v[128:131], v99 offset:19392
	s_waitcnt lgkmcnt(6)
	s_nop 0
	v_fma_f32 v144, v100, v140, v142
	v_fmac_f32_e64 v144, v101, v96
	v_cndmask_b32_e64 v145, v96, v144, s[10:11]
	v_cndmask_b32_e64 v145, v145, v140, s[8:9]
	v_fma_f32 v50, v102, v140, v143
	v_fmac_f32_e64 v50, v103, v96
	v_mfma_f32_16x16x4_f32 v[64:67], v92, v145, v[64:67]
	v_mfma_f32_16x16x4_f32 v[60:63], v93, v145, v[60:63]
	v_mfma_f32_16x16x4_f32 v[52:55], v94, v145, v[52:55]
	v_mfma_f32_16x16x4_f32 v[56:59], v95, v145, v[56:59]
	v_cndmask_b32_e64 v50, v50, v141, s[8:9]
	ds_write_b32 v3, v50 offset:5120
	v_add_u32_e32 v0, 0x400, v0
	ds_read2_b32 v[132:133], v0 offset1:16
	ds_read2_b32 v[134:135], v0 offset0:32 offset1:48
	ds_read_b32 v97, v1 offset:5632
	ds_read_b128 v[136:139], v2 offset:176
	v_cvt_pk_bf16_f32 v8, v64, v65
	v_cvt_pk_bf16_f32 v9, v66, v67
	v_cvt_pk_bf16_f32 v10, v60, v61
	v_cvt_pk_bf16_f32 v11, v62, v63
	v_cvt_pk_bf16_f32 v12, v52, v53
	v_cvt_pk_bf16_f32 v13, v54, v55
	s_waitcnt lgkmcnt(4)
	s_nop 0
	v_mfma_f32_16x16x32_bf16 v[140:143], v[104:107], v[8:11], 0
	v_cvt_pk_bf16_f32 v14, v56, v57
	v_cvt_pk_bf16_f32 v15, v58, v59
	v_pk_mul_f32 v[64:65], v[64:65], v[112:113]
	v_pk_mul_f32 v[66:67], v[66:67], v[114:115]
	v_mfma_f32_16x16x32_bf16 v[140:143], v[108:111], v[12:15], v[140:143]
	v_pk_mul_f32 v[60:61], v[60:61], v[116:117]
	v_pk_mul_f32 v[62:63], v[62:63], v[118:119]
	v_pk_mul_f32 v[52:53], v[52:53], v[120:121]
	v_pk_mul_f32 v[54:55], v[54:55], v[122:123]
	v_pk_mul_f32 v[56:57], v[56:57], v[128:129]
	v_pk_mul_f32 v[58:59], v[58:59], v[130:131]
	ds_read_b128 v[68:71], v98 offset:6144
	ds_read_b128 v[72:75], v98 offset:6208
	ds_read_b128 v[76:79], v99 offset:19456
	ds_read_b128 v[80:83], v99 offset:19520
	ds_read_b128 v[84:87], v99 offset:19584
	ds_read_b128 v[88:91], v99 offset:19648
	s_waitcnt lgkmcnt(6)
; __device__ __forceinline__ void scan_head(const Params& p, LAS unsigned char* lds, int bh, const int wave) {
;     ...
;             bf16x8 Pa0, Pa1, Qa0, Qa1; f32x4 Pw0, Pw1, Pw2, Pw3, Qw0, Qw1, Qw2, Qw3, Pcs, Qcs; float Pb0, Pb1, Pb2, Pb3, Pvt, Pvu, Qb0, Qb1, Qb2, Qb3, Qvt, Qvu;
;             SCAN_LD(P, 0);
; #pragma unroll 1
;             for (int pi = 0; pi < 16; pi += 2) {
;                 SCAN_LD(Q, pi + 1);
;                 SCAN_STEP(P, pi);
;                 if (pi + 2 < 16) SCAN_LD(P, pi + 2);
;                 SCAN_STEP(Q, pi + 1);
	s_nop 0
	v_fma_f32 v144, v136, v140, v142
	v_fmac_f32_e64 v144, v137, v97
	v_cndmask_b32_e64 v145, v97, v144, s[10:11]
	v_cndmask_b32_e64 v145, v145, v140, s[8:9]
	v_fma_f32 v50, v138, v140, v143
	v_fmac_f32_e64 v50, v139, v97
	v_mfma_f32_16x16x4_f32 v[64:67], v132, v145, v[64:67]
	v_mfma_f32_16x16x4_f32 v[60:63], v133, v145, v[60:63]
	v_mfma_f32_16x16x4_f32 v[52:55], v134, v145, v[52:55]
	v_mfma_f32_16x16x4_f32 v[56:59], v135, v145, v[56:59]
	v_cndmask_b32_e64 v50, v50, v141, s[8:9]
	ds_write_b32 v3, v50 offset:5632
	v_add_u32_e32 v0, 0x400, v0
	ds_read2_b32 v[92:93], v0 offset1:16
	ds_read2_b32 v[94:95], v0 offset0:32 offset1:48
	ds_read_b32 v96, v1 offset:6144
	ds_read_b128 v[100:103], v2 offset:192
	v_cvt_pk_bf16_f32 v8, v64, v65
	v_cvt_pk_bf16_f32 v9, v66, v67
	v_cvt_pk_bf16_f32 v10, v60, v61
	v_cvt_pk_bf16_f32 v11, v62, v63
	v_cvt_pk_bf16_f32 v12, v52, v53
	v_cvt_pk_bf16_f32 v13, v54, v55
	s_waitcnt lgkmcnt(4)
	s_nop 0
	v_mfma_f32_16x16x32_bf16 v[140:143], v[68:71], v[8:11], 0
	v_cvt_pk_bf16_f32 v14, v56, v57
	v_cvt_pk_bf16_f32 v15, v58, v59
	v_pk_mul_f32 v[64:65], v[64:65], v[76:77]
	v_pk_mul_f32 v[66:67], v[66:67], v[78:79]
	v_mfma_f32_16x16x32_bf16 v[140:143], v[72:75], v[12:15], v[140:143]
	v_pk_mul_f32 v[60:61], v[60:61], v[80:81]
	v_pk_mul_f32 v[62:63], v[62:63], v[82:83]
	v_pk_mul_f32 v[52:53], v[52:53], v[84:85]
	v_pk_mul_f32 v[54:55], v[54:55], v[86:87]
	v_pk_mul_f32 v[56:57], v[56:57], v[88:89]
	v_pk_mul_f32 v[58:59], v[58:59], v[90:91]
	ds_read_b128 v[104:107], v98 offset:6656
	ds_read_b128 v[108:111], v98 offset:6720
	ds_read_b128 v[112:115], v99 offset:19712
	ds_read_b128 v[116:119], v99 offset:19776
	ds_read_b128 v[120:123], v99 offset:19840
	ds_read_b128 v[128:131], v99 offset:19904
	s_waitcnt lgkmcnt(6)
	s_nop 0
	v_fma_f32 v144, v100, v140, v142
	v_fmac_f32_e64 v144, v101, v96
	v_cndmask_b32_e64 v145, v96, v144, s[10:11]
	v_cndmask_b32_e64 v145, v145, v140, s[8:9]
	v_fma_f32 v50, v102, v140, v143
	v_fmac_f32_e64 v50, v103, v96
	v_mfma_f32_16x16x4_f32 v[64:67], v92, v145, v[64:67]
	v_mfma_f32_16x16x4_f32 v[60:63], v93, v145, v[60:63]
	v_mfma_f32_16x16x4_f32 v[52:55], v94, v145, v[52:55]
	v_mfma_f32_16x16x4_f32 v[56:59], v95, v145, v[56:59]
	v_cndmask_b32_e64 v50, v50, v141, s[8:9]
	ds_write_b32 v3, v50 offset:6144
	v_add_u32_e32 v0, 0x400, v0
	ds_read2_b32 v[132:133], v0 offset1:16
	ds_read2_b32 v[134:135], v0 offset0:32 offset1:48
	ds_read_b32 v97, v1 offset:6656
	ds_read_b128 v[136:139], v2 offset:208
	v_cvt_pk_bf16_f32 v8, v64, v65
	v_cvt_pk_bf16_f32 v9, v66, v67
	v_cvt_pk_bf16_f32 v10, v60, v61
	v_cvt_pk_bf16_f32 v11, v62, v63
	v_cvt_pk_bf16_f32 v12, v52, v53
	v_cvt_pk_bf16_f32 v13, v54, v55
	s_waitcnt lgkmcnt(4)
	s_nop 0
	v_mfma_f32_16x16x32_bf16 v[140:143], v[104:107], v[8:11], 0
	v_cvt_pk_bf16_f32 v14, v56, v57
	v_cvt_pk_bf16_f32 v15, v58, v59
	v_pk_mul_f32 v[64:65], v[64:65], v[112:113]
	v_pk_mul_f32 v[66:67], v[66:67], v[114:115]
	v_mfma_f32_16x16x32_bf16 v[140:143], v[108:111], v[12:15], v[140:143]
	v_pk_mul_f32 v[60:61], v[60:61], v[116:117]
	v_pk_mul_f32 v[62:63], v[62:63], v[118:119]
	v_pk_mul_f32 v[52:53], v[52:53], v[120:121]
	v_pk_mul_f32 v[54:55], v[54:55], v[122:123]
	v_pk_mul_f32 v[56:57], v[56:57], v[128:129]
	v_pk_mul_f32 v[58:59], v[58:59], v[130:131]
	ds_read_b128 v[68:71], v98 offset:7168
	ds_read_b128 v[72:75], v98 offset:7232
	ds_read_b128 v[76:79], v99 offset:19968
	ds_read_b128 v[80:83], v99 offset:20032
	ds_read_b128 v[84:87], v99 offset:20096
	ds_read_b128 v[88:91], v99 offset:20160
	s_waitcnt lgkmcnt(6)
; __device__ __forceinline__ void scan_head(const Params& p, LAS unsigned char* lds, int bh, const int wave) {
;     ...
;             bf16x8 Pa0, Pa1, Qa0, Qa1; f32x4 Pw0, Pw1, Pw2, Pw3, Qw0, Qw1, Qw2, Qw3, Pcs, Qcs; float Pb0, Pb1, Pb2, Pb3, Pvt, Pvu, Qb0, Qb1, Qb2, Qb3, Qvt, Qvu;
;             SCAN_LD(P, 0);
; #pragma unroll 1
;             for (int pi = 0; pi < 16; pi += 2) {
;                 SCAN_LD(Q, pi + 1);
;                 SCAN_STEP(P, pi);
;                 if (pi + 2 < 16) SCAN_LD(P, pi + 2);
;                 SCAN_STEP(Q, pi + 1);
;             }
	s_nop 0
	v_fma_f32 v144, v136, v140, v142
	v_fmac_f32_e64 v144, v137, v97
	v_cndmask_b32_e64 v145, v97, v144, s[10:11]
	v_cndmask_b32_e64 v145, v145, v140, s[8:9]
	v_fma_f32 v50, v138, v140, v143
	v_fmac_f32_e64 v50, v139, v97
	v_mfma_f32_16x16x4_f32 v[64:67], v132, v145, v[64:67]
	v_mfma_f32_16x16x4_f32 v[60:63], v133, v145, v[60:63]
	v_mfma_f32_16x16x4_f32 v[52:55], v134, v145, v[52:55]
	v_mfma_f32_16x16x4_f32 v[56:59], v135, v145, v[56:59]
	v_cndmask_b32_e64 v50, v50, v141, s[8:9]
	ds_write_b32 v3, v50 offset:6656
	v_add_u32_e32 v0, 0x400, v0
	ds_read2_b32 v[92:93], v0 offset1:16
	ds_read2_b32 v[94:95], v0 offset0:32 offset1:48
	ds_read_b32 v96, v1 offset:7168
	ds_read_b128 v[100:103], v2 offset:224
	v_cvt_pk_bf16_f32 v8, v64, v65
	v_cvt_pk_bf16_f32 v9, v66, v67
	v_cvt_pk_bf16_f32 v10, v60, v61
	v_cvt_pk_bf16_f32 v11, v62, v63
	v_cvt_pk_bf16_f32 v12, v52, v53
	v_cvt_pk_bf16_f32 v13, v54, v55
	s_waitcnt lgkmcnt(4)
	s_nop 0
	v_mfma_f32_16x16x32_bf16 v[140:143], v[68:71], v[8:11], 0
	v_cvt_pk_bf16_f32 v14, v56, v57
	v_cvt_pk_bf16_f32 v15, v58, v59
	v_pk_mul_f32 v[64:65], v[64:65], v[76:77]
	v_pk_mul_f32 v[66:67], v[66:67], v[78:79]
	v_mfma_f32_16x16x32_bf16 v[140:143], v[72:75], v[12:15], v[140:143]
	v_pk_mul_f32 v[60:61], v[60:61], v[80:81]
	v_pk_mul_f32 v[62:63], v[62:63], v[82:83]
	v_pk_mul_f32 v[52:53], v[52:53], v[84:85]
	v_pk_mul_f32 v[54:55], v[54:55], v[86:87]
	v_pk_mul_f32 v[56:57], v[56:57], v[88:89]
	v_pk_mul_f32 v[58:59], v[58:59], v[90:91]
	ds_read_b128 v[104:107], v98 offset:7680
	ds_read_b128 v[108:111], v98 offset:7744
	ds_read_b128 v[112:115], v99 offset:20224
	ds_read_b128 v[116:119], v99 offset:20288
	ds_read_b128 v[120:123], v99 offset:20352
	ds_read_b128 v[128:131], v99 offset:20416
	s_waitcnt lgkmcnt(6)
	s_nop 0
	v_fma_f32 v144, v100, v140, v142
	v_fmac_f32_e64 v144, v101, v96
	v_cndmask_b32_e64 v145, v96, v144, s[10:11]
	v_cndmask_b32_e64 v145, v145, v140, s[8:9]
	v_fma_f32 v50, v102, v140, v143
	v_fmac_f32_e64 v50, v103, v96
	v_mfma_f32_16x16x4_f32 v[64:67], v92, v145, v[64:67]
	v_mfma_f32_16x16x4_f32 v[60:63], v93, v145, v[60:63]
	v_mfma_f32_16x16x4_f32 v[52:55], v94, v145, v[52:55]
	v_mfma_f32_16x16x4_f32 v[56:59], v95, v145, v[56:59]
	v_cndmask_b32_e64 v50, v50, v141, s[8:9]
	ds_write_b32 v3, v50 offset:7168
	v_add_u32_e32 v0, 0x400, v0
	ds_read2_b32 v[132:133], v0 offset1:16
	ds_read2_b32 v[134:135], v0 offset0:32 offset1:48
	ds_read_b32 v97, v1 offset:7680
	ds_read_b128 v[136:139], v2 offset:240
	v_cvt_pk_bf16_f32 v8, v64, v65
	v_cvt_pk_bf16_f32 v9, v66, v67
	v_cvt_pk_bf16_f32 v10, v60, v61
	v_cvt_pk_bf16_f32 v11, v62, v63
	v_cvt_pk_bf16_f32 v12, v52, v53
	v_cvt_pk_bf16_f32 v13, v54, v55
	s_waitcnt lgkmcnt(4)
	s_nop 0
	v_mfma_f32_16x16x32_bf16 v[140:143], v[104:107], v[8:11], 0
	v_cvt_pk_bf16_f32 v14, v56, v57
	v_cvt_pk_bf16_f32 v15, v58, v59
	v_pk_mul_f32 v[64:65], v[64:65], v[112:113]
	v_pk_mul_f32 v[66:67], v[66:67], v[114:115]
	v_mfma_f32_16x16x32_bf16 v[140:143], v[108:111], v[12:15], v[140:143]
	v_pk_mul_f32 v[60:61], v[60:61], v[116:117]
	v_pk_mul_f32 v[62:63], v[62:63], v[118:119]
	v_pk_mul_f32 v[52:53], v[52:53], v[120:121]
	v_pk_mul_f32 v[54:55], v[54:55], v[122:123]
	v_pk_mul_f32 v[56:57], v[56:57], v[128:129]
	v_pk_mul_f32 v[58:59], v[58:59], v[130:131]
	s_waitcnt lgkmcnt(0)
	s_nop 1
	v_fma_f32 v144, v136, v140, v142
	v_fmac_f32_e64 v144, v137, v97
	v_cndmask_b32_e64 v145, v97, v144, s[10:11]
	v_cndmask_b32_e64 v145, v145, v140, s[8:9]
	v_fma_f32 v50, v138, v140, v143
	v_fmac_f32_e64 v50, v139, v97
	v_mfma_f32_16x16x4_f32 v[64:67], v132, v145, v[64:67]
	v_mfma_f32_16x16x4_f32 v[60:63], v133, v145, v[60:63]
	v_mfma_f32_16x16x4_f32 v[52:55], v134, v145, v[52:55]
	v_mfma_f32_16x16x4_f32 v[56:59], v135, v145, v[56:59]
	v_cndmask_b32_e64 v50, v50, v141, s[8:9]
	ds_write_b32 v3, v50 offset:7680
	s_nop 7
	s_nop 0
